# moe_tables: all 64 expert counters requested together (one round trip instead of ~38 dependent ones) at the start of the first expert GEMM phase
# speedup vs baseline: 1.0165x; 1.0010x over previous
; #define LAS __attribute__((address_space(3)))
; DEV void moe_tables(const Params& p, int layer, LAS int* bs, LAS int* cn) {
;     const unsigned* cnt = (const unsigned*)(p.ws + WS_CTL) + CW_CNT + 2048 * layer;
;     if (threadIdx.x == 0) { int a = 0; for (int e = 0; e < 64; ++e) { const int c = (int)cnt[e * 32]; cn[e] = c; bs[e] = a; a += (c + MOE_RB - 1) / MOE_RB; } bs[64] = a; }
;     __syncthreads();
.LBB0_1299:
	s_andn2_b64 vcc, exec, s[4:5]
	s_cbranch_vccnz .LBB0_1387
	v_readlane_b32 s4, v252, 1
	v_readlane_b32 s5, v252, 2
	s_load_dwordx2 s[6:7], s[4:5], 0xe0
	v_readlane_b32 s2, v254, 26
	v_readlane_b32 s3, v254, 27
	s_waitcnt lgkmcnt(0)
	s_mov_b64 s[4:5], s[6:7]
	s_mov_b64 s[8:9], s[6:7]
	s_and_saveexec_b64 s[4:5], s[2:3]
	s_cbranch_execz .LBB0_1302
	s_lshl_b32 s30, s72, 11
	s_lshl_b64 s[12:13], s[30:31], 2
	s_add_u32 s6, s6, s12
	s_addc_u32 s7, s7, s13
	v_mov_b32_e32 v2, 0x4000
	global_load_dword v2, v2, s[6:7]
	s_add_u32 s38, s6, 0x4000
	s_addc_u32 s39, s7, 0
	v_readlane_b32 s2, v253, 57
	v_mov_b32_e32 v11, 0x5000
	global_load_dword v130, v179, s[38:39] offset:128
	global_load_dword v131, v179, s[38:39] offset:256
	global_load_dword v132, v179, s[38:39] offset:384
	global_load_dword v133, v179, s[38:39] offset:512
	global_load_dword v134, v179, s[38:39] offset:640
	global_load_dword v135, v179, s[38:39] offset:768
	global_load_dword v136, v179, s[38:39] offset:896
	global_load_dword v137, v179, s[38:39] offset:1024
	global_load_dword v138, v179, s[38:39] offset:1152
	global_load_dword v142, v179, s[38:39] offset:1280
	global_load_dword v143, v179, s[38:39] offset:1408
	global_load_dword v144, v179, s[38:39] offset:1536
	global_load_dword v145, v179, s[38:39] offset:1664
	global_load_dword v148, v179, s[38:39] offset:1792
	global_load_dword v149, v179, s[38:39] offset:1920
	global_load_dword v150, v179, s[38:39] offset:2048
	global_load_dword v151, v179, s[38:39] offset:2176
	global_load_dword v152, v179, s[38:39] offset:2304
	global_load_dword v153, v179, s[38:39] offset:2432
	global_load_dword v154, v179, s[38:39] offset:2560
	global_load_dword v155, v179, s[38:39] offset:2688
	global_load_dword v156, v179, s[38:39] offset:2816
	global_load_dword v157, v179, s[38:39] offset:2944
	global_load_dword v158, v179, s[38:39] offset:3072
	global_load_dword v159, v179, s[38:39] offset:3200
	global_load_dword v160, v179, s[38:39] offset:3328
	global_load_dword v161, v179, s[38:39] offset:3456
	global_load_dword v162, v179, s[38:39] offset:3584
	global_load_dword v163, v179, s[38:39] offset:3712
	global_load_dword v164, v179, s[38:39] offset:3840
	global_load_dword v165, v179, s[38:39] offset:3968
	global_load_dword v166, v11, s[6:7]
	global_load_dword v167, v11, s[6:7] offset:128
	global_load_dword v168, v11, s[6:7] offset:256
	global_load_dword v169, v11, s[6:7] offset:384
	global_load_dword v170, v11, s[6:7] offset:512
	global_load_dword v171, v11, s[6:7] offset:640
	global_load_dword v172, v11, s[6:7] offset:768
	global_load_dword v173, v11, s[6:7] offset:896
	global_load_dword v174, v11, s[6:7] offset:1024
	global_load_dword v175, v11, s[6:7] offset:1152
	global_load_dword v176, v11, s[6:7] offset:1280
	global_load_dword v177, v11, s[6:7] offset:1408
	global_load_dword v180, v11, s[6:7] offset:1536
	global_load_dword v181, v11, s[6:7] offset:1664
	global_load_dword v182, v11, s[6:7] offset:1792
	global_load_dword v183, v11, s[6:7] offset:1920
	global_load_dword v184, v11, s[6:7] offset:2048
	global_load_dword v185, v11, s[6:7] offset:2176
	global_load_dword v186, v11, s[6:7] offset:2304
	global_load_dword v188, v11, s[6:7] offset:2432
	global_load_dword v189, v11, s[6:7] offset:2560
	global_load_dword v198, v11, s[6:7] offset:2688
	global_load_dword v199, v11, s[6:7] offset:2816
	global_load_dword v200, v11, s[6:7] offset:2944
	global_load_dword v201, v11, s[6:7] offset:3072
	global_load_dword v202, v11, s[6:7] offset:3200
	global_load_dword v203, v11, s[6:7] offset:3328
	global_load_dword v204, v11, s[6:7] offset:3456
	global_load_dword v205, v11, s[6:7] offset:3584
	global_load_dword v206, v11, s[6:7] offset:3712
	global_load_dword v207, v11, s[6:7] offset:3840
	global_load_dword v210, v11, s[6:7] offset:3968
	s_waitcnt vmcnt(0)
	v_add_u32_e32 v3, 0xff, v2
	v_ashrrev_i32_e32 v4, 31, v3
	v_add_u32_sdwa v3, v3, v4 dst_sel:DWORD dst_unused:UNUSED_PAD src0_sel:DWORD src1_sel:BYTE_3
	v_ashrrev_i32_e32 v7, 8, v3
	v_mov_b32_e32 v3, v130
	s_waitcnt vmcnt(0)
	v_add_u32_e32 v4, 0xff, v3
	v_ashrrev_i32_e32 v5, 31, v4
	v_add_u32_sdwa v4, v4, v5 dst_sel:DWORD dst_unused:UNUSED_PAD src0_sel:DWORD src1_sel:BYTE_3
	v_ashrrev_i32_e32 v4, 8, v4
	v_add_u32_e32 v8, v4, v7
	v_mov_b32_e32 v4, v131
	s_waitcnt vmcnt(0)
	v_add_u32_e32 v5, 0xff, v4
	v_ashrrev_i32_e32 v6, 31, v5
	v_add_u32_sdwa v5, v5, v6 dst_sel:DWORD dst_unused:UNUSED_PAD src0_sel:DWORD src1_sel:BYTE_3
	v_ashrrev_i32_e32 v5, 8, v5
	v_add_u32_e32 v9, v5, v8
	v_mov_b32_e32 v5, v132
	v_mov_b32_e32 v6, s2
	v_readlane_b32 s2, v253, 58
	s_waitcnt vmcnt(0)
	ds_write_b128 v6, v[2:5]
	v_mov_b32_e32 v6, v179
	v_mov_b32_e32 v2, s2
	ds_write_b128 v2, v[6:9]
	v_mov_b32_e32 v6, v133
	v_mov_b32_e32 v7, v134
	v_mov_b32_e32 v8, v135
	v_add_u32_e32 v2, 0xff, v5
	v_ashrrev_i32_e32 v3, 31, v2
	v_add_u32_sdwa v2, v2, v3 dst_sel:DWORD dst_unused:UNUSED_PAD src0_sel:DWORD src1_sel:BYTE_3
	v_ashrrev_i32_e32 v2, 8, v2
	v_add_u32_e32 v2, v2, v9
	v_readlane_b32 s2, v253, 59
	s_waitcnt vmcnt(2)
	v_add_u32_e32 v3, 0xff, v6
	v_ashrrev_i32_e32 v4, 31, v3
	v_add_u32_sdwa v3, v3, v4 dst_sel:DWORD dst_unused:UNUSED_PAD src0_sel:DWORD src1_sel:BYTE_3
	s_waitcnt vmcnt(1)
	v_add_u32_e32 v4, 0xff, v7
	v_ashrrev_i32_e32 v5, 31, v4
	v_add_u32_sdwa v4, v4, v5 dst_sel:DWORD dst_unused:UNUSED_PAD src0_sel:DWORD src1_sel:BYTE_3
	s_waitcnt vmcnt(0)
	v_add_u32_e32 v5, 0xff, v8
	v_ashrrev_i32_e32 v9, 31, v5
	v_add_u32_sdwa v5, v5, v9 dst_sel:DWORD dst_unused:UNUSED_PAD src0_sel:DWORD src1_sel:BYTE_3
	v_mov_b32_e32 v9, v136
	v_ashrrev_i32_e32 v3, 8, v3
	v_add_u32_e32 v3, v3, v2
	v_ashrrev_i32_e32 v4, 8, v4
	v_add_u32_e32 v4, v4, v3
	v_ashrrev_i32_e32 v5, 8, v5
	v_mov_b32_e32 v10, s2
	v_readlane_b32 s2, v253, 60
	v_add_u32_e32 v5, v5, v4
	s_waitcnt vmcnt(0)
; DEV void moe_tables(const Params& p, int layer, LAS int* bs, LAS int* cn) {
;     ...
;     if (threadIdx.x == 0) { int a = 0; for (int e = 0; e < 64; ++e) { const int c = (int)cnt[e * 32]; cn[e] = c; bs[e] = a; a += (c + MOE_RB - 1) / MOE_RB; } bs[64] = a; }
	ds_write_b128 v10, v[6:9]
	v_mov_b32_e32 v6, s2
	ds_write_b128 v6, v[2:5]
	v_mov_b32_e32 v6, v137
	v_mov_b32_e32 v7, v138
	v_mov_b32_e32 v8, v142
	v_add_u32_e32 v2, 0xff, v9
	v_ashrrev_i32_e32 v3, 31, v2
	v_add_u32_sdwa v2, v2, v3 dst_sel:DWORD dst_unused:UNUSED_PAD src0_sel:DWORD src1_sel:BYTE_3
	v_ashrrev_i32_e32 v2, 8, v2
	v_add_u32_e32 v2, v2, v5
	v_readlane_b32 s2, v253, 61
	s_waitcnt vmcnt(2)
	v_add_u32_e32 v3, 0xff, v6
	v_ashrrev_i32_e32 v4, 31, v3
	v_add_u32_sdwa v3, v3, v4 dst_sel:DWORD dst_unused:UNUSED_PAD src0_sel:DWORD src1_sel:BYTE_3
	s_waitcnt vmcnt(1)
	v_add_u32_e32 v4, 0xff, v7
	v_ashrrev_i32_e32 v5, 31, v4
	v_add_u32_sdwa v4, v4, v5 dst_sel:DWORD dst_unused:UNUSED_PAD src0_sel:DWORD src1_sel:BYTE_3
	s_waitcnt vmcnt(0)
	v_add_u32_e32 v5, 0xff, v8
	v_ashrrev_i32_e32 v9, 31, v5
	v_add_u32_sdwa v5, v5, v9 dst_sel:DWORD dst_unused:UNUSED_PAD src0_sel:DWORD src1_sel:BYTE_3
	v_mov_b32_e32 v9, v143
	v_ashrrev_i32_e32 v3, 8, v3
	v_add_u32_e32 v3, v3, v2
	v_ashrrev_i32_e32 v4, 8, v4
	v_add_u32_e32 v4, v4, v3
	v_ashrrev_i32_e32 v5, 8, v5
	v_mov_b32_e32 v10, s2
	v_readlane_b32 s2, v253, 62
	v_add_u32_e32 v5, v5, v4
	s_waitcnt vmcnt(0)
	ds_write_b128 v10, v[6:9]
	v_mov_b32_e32 v6, s2
	ds_write_b128 v6, v[2:5]
	v_mov_b32_e32 v6, v144
	v_mov_b32_e32 v7, v145
	v_mov_b32_e32 v8, v148
	v_add_u32_e32 v2, 0xff, v9
	v_ashrrev_i32_e32 v3, 31, v2
	v_add_u32_sdwa v2, v2, v3 dst_sel:DWORD dst_unused:UNUSED_PAD src0_sel:DWORD src1_sel:BYTE_3
	v_ashrrev_i32_e32 v2, 8, v2
	v_add_u32_e32 v2, v2, v5
	v_readlane_b32 s2, v253, 63
	s_waitcnt vmcnt(2)
	v_add_u32_e32 v3, 0xff, v6
	v_ashrrev_i32_e32 v4, 31, v3
	v_add_u32_sdwa v3, v3, v4 dst_sel:DWORD dst_unused:UNUSED_PAD src0_sel:DWORD src1_sel:BYTE_3
	s_waitcnt vmcnt(1)
	v_add_u32_e32 v4, 0xff, v7
	v_ashrrev_i32_e32 v5, 31, v4
	v_add_u32_sdwa v4, v4, v5 dst_sel:DWORD dst_unused:UNUSED_PAD src0_sel:DWORD src1_sel:BYTE_3
	s_waitcnt vmcnt(0)
	v_add_u32_e32 v5, 0xff, v8
	v_ashrrev_i32_e32 v9, 31, v5
	v_add_u32_sdwa v5, v5, v9 dst_sel:DWORD dst_unused:UNUSED_PAD src0_sel:DWORD src1_sel:BYTE_3
	v_mov_b32_e32 v9, v149
	v_ashrrev_i32_e32 v3, 8, v3
	v_add_u32_e32 v3, v3, v2
	v_ashrrev_i32_e32 v4, 8, v4
	v_add_u32_e32 v4, v4, v3
	v_ashrrev_i32_e32 v5, 8, v5
	v_mov_b32_e32 v10, s2
	v_readlane_b32 s2, v254, 0
	v_add_u32_e32 v5, v5, v4
	s_waitcnt vmcnt(0)
	ds_write_b128 v10, v[6:9]
	v_mov_b32_e32 v6, s2
	ds_write_b128 v6, v[2:5]
	v_mov_b32_e32 v6, v150
	v_mov_b32_e32 v7, v151
	v_mov_b32_e32 v8, v152
	v_add_u32_e32 v2, 0xff, v9
	v_ashrrev_i32_e32 v3, 31, v2
	v_add_u32_sdwa v2, v2, v3 dst_sel:DWORD dst_unused:UNUSED_PAD src0_sel:DWORD src1_sel:BYTE_3
	v_ashrrev_i32_e32 v2, 8, v2
	v_add_u32_e32 v2, v2, v5
	v_readlane_b32 s2, v254, 1
	s_waitcnt vmcnt(2)
	v_add_u32_e32 v3, 0xff, v6
	v_ashrrev_i32_e32 v4, 31, v3
	v_add_u32_sdwa v3, v3, v4 dst_sel:DWORD dst_unused:UNUSED_PAD src0_sel:DWORD src1_sel:BYTE_3
	s_waitcnt vmcnt(1)
	v_add_u32_e32 v4, 0xff, v7
	v_ashrrev_i32_e32 v5, 31, v4
	v_add_u32_sdwa v4, v4, v5 dst_sel:DWORD dst_unused:UNUSED_PAD src0_sel:DWORD src1_sel:BYTE_3
	s_waitcnt vmcnt(0)
	v_add_u32_e32 v5, 0xff, v8
	v_ashrrev_i32_e32 v9, 31, v5
	v_add_u32_sdwa v5, v5, v9 dst_sel:DWORD dst_unused:UNUSED_PAD src0_sel:DWORD src1_sel:BYTE_3
	v_mov_b32_e32 v9, v153
	v_ashrrev_i32_e32 v3, 8, v3
	v_add_u32_e32 v3, v3, v2
	v_ashrrev_i32_e32 v4, 8, v4
	v_add_u32_e32 v4, v4, v3
	v_ashrrev_i32_e32 v5, 8, v5
	v_mov_b32_e32 v10, s2
	v_readlane_b32 s2, v254, 2
	v_add_u32_e32 v5, v5, v4
	s_waitcnt vmcnt(0)
	ds_write_b128 v10, v[6:9]
	v_mov_b32_e32 v6, s2
	ds_write_b128 v6, v[2:5]
	v_mov_b32_e32 v6, v154
	v_mov_b32_e32 v7, v155
	v_mov_b32_e32 v8, v156
	v_add_u32_e32 v2, 0xff, v9
	v_ashrrev_i32_e32 v3, 31, v2
	v_add_u32_sdwa v2, v2, v3 dst_sel:DWORD dst_unused:UNUSED_PAD src0_sel:DWORD src1_sel:BYTE_3
	v_ashrrev_i32_e32 v2, 8, v2
	v_add_u32_e32 v2, v2, v5
	v_readlane_b32 s2, v254, 3
	s_waitcnt vmcnt(2)
	v_add_u32_e32 v3, 0xff, v6
	v_ashrrev_i32_e32 v4, 31, v3
	v_add_u32_sdwa v3, v3, v4 dst_sel:DWORD dst_unused:UNUSED_PAD src0_sel:DWORD src1_sel:BYTE_3
	s_waitcnt vmcnt(1)
	v_add_u32_e32 v4, 0xff, v7
	v_ashrrev_i32_e32 v5, 31, v4
	v_add_u32_sdwa v4, v4, v5 dst_sel:DWORD dst_unused:UNUSED_PAD src0_sel:DWORD src1_sel:BYTE_3
	s_waitcnt vmcnt(0)
	v_add_u32_e32 v5, 0xff, v8
	v_ashrrev_i32_e32 v9, 31, v5
	v_add_u32_sdwa v5, v5, v9 dst_sel:DWORD dst_unused:UNUSED_PAD src0_sel:DWORD src1_sel:BYTE_3
	v_mov_b32_e32 v9, v157
	v_ashrrev_i32_e32 v3, 8, v3
	v_add_u32_e32 v3, v3, v2
	v_ashrrev_i32_e32 v4, 8, v4
	v_add_u32_e32 v4, v4, v3
	v_ashrrev_i32_e32 v5, 8, v5
	v_mov_b32_e32 v10, s2
	v_readlane_b32 s2, v254, 4
	v_add_u32_e32 v5, v5, v4
	s_waitcnt vmcnt(0)
	ds_write_b128 v10, v[6:9]
	v_mov_b32_e32 v6, s2
	ds_write_b128 v6, v[2:5]
	v_mov_b32_e32 v6, v158
	v_mov_b32_e32 v7, v159
	v_mov_b32_e32 v8, v160
	v_add_u32_e32 v2, 0xff, v9
	v_ashrrev_i32_e32 v3, 31, v2
	v_add_u32_sdwa v2, v2, v3 dst_sel:DWORD dst_unused:UNUSED_PAD src0_sel:DWORD src1_sel:BYTE_3
	v_ashrrev_i32_e32 v2, 8, v2
	v_add_u32_e32 v2, v2, v5
	v_readlane_b32 s2, v254, 5
	s_waitcnt vmcnt(2)
	v_add_u32_e32 v3, 0xff, v6
	v_ashrrev_i32_e32 v4, 31, v3
	v_add_u32_sdwa v3, v3, v4 dst_sel:DWORD dst_unused:UNUSED_PAD src0_sel:DWORD src1_sel:BYTE_3
	s_waitcnt vmcnt(1)
	v_add_u32_e32 v4, 0xff, v7
	v_ashrrev_i32_e32 v5, 31, v4
	v_add_u32_sdwa v4, v4, v5 dst_sel:DWORD dst_unused:UNUSED_PAD src0_sel:DWORD src1_sel:BYTE_3
	s_waitcnt vmcnt(0)
	v_add_u32_e32 v5, 0xff, v8
	v_ashrrev_i32_e32 v9, 31, v5
	v_add_u32_sdwa v5, v5, v9 dst_sel:DWORD dst_unused:UNUSED_PAD src0_sel:DWORD src1_sel:BYTE_3
	v_mov_b32_e32 v9, v161
	v_ashrrev_i32_e32 v3, 8, v3
	v_add_u32_e32 v3, v3, v2
	v_ashrrev_i32_e32 v4, 8, v4
	v_add_u32_e32 v4, v4, v3
	v_ashrrev_i32_e32 v5, 8, v5
	v_mov_b32_e32 v10, s2
	v_readlane_b32 s2, v254, 6
	v_add_u32_e32 v5, v5, v4
	s_waitcnt vmcnt(0)
; DEV void moe_tables(const Params& p, int layer, LAS int* bs, LAS int* cn) {
;     ...
;     if (threadIdx.x == 0) { int a = 0; for (int e = 0; e < 64; ++e) { const int c = (int)cnt[e * 32]; cn[e] = c; bs[e] = a; a += (c + MOE_RB - 1) / MOE_RB; } bs[64] = a; }
	ds_write_b128 v10, v[6:9]
	v_mov_b32_e32 v6, s2
	ds_write_b128 v6, v[2:5]
	v_mov_b32_e32 v6, v162
	v_mov_b32_e32 v7, v163
	v_mov_b32_e32 v8, v164
	v_add_u32_e32 v2, 0xff, v9
	v_ashrrev_i32_e32 v3, 31, v2
	v_add_u32_sdwa v2, v2, v3 dst_sel:DWORD dst_unused:UNUSED_PAD src0_sel:DWORD src1_sel:BYTE_3
	v_ashrrev_i32_e32 v2, 8, v2
	v_add_u32_e32 v2, v2, v5
	v_readlane_b32 s2, v254, 7
	s_waitcnt vmcnt(2)
	v_add_u32_e32 v3, 0xff, v6
	v_ashrrev_i32_e32 v4, 31, v3
	v_add_u32_sdwa v3, v3, v4 dst_sel:DWORD dst_unused:UNUSED_PAD src0_sel:DWORD src1_sel:BYTE_3
	s_waitcnt vmcnt(1)
	v_add_u32_e32 v4, 0xff, v7
	v_ashrrev_i32_e32 v5, 31, v4
	v_add_u32_sdwa v4, v4, v5 dst_sel:DWORD dst_unused:UNUSED_PAD src0_sel:DWORD src1_sel:BYTE_3
	s_waitcnt vmcnt(0)
	v_add_u32_e32 v5, 0xff, v8
	v_ashrrev_i32_e32 v9, 31, v5
	v_add_u32_sdwa v5, v5, v9 dst_sel:DWORD dst_unused:UNUSED_PAD src0_sel:DWORD src1_sel:BYTE_3
	v_mov_b32_e32 v9, v165
	v_ashrrev_i32_e32 v3, 8, v3
	v_add_u32_e32 v3, v3, v2
	v_ashrrev_i32_e32 v4, 8, v4
	v_add_u32_e32 v4, v4, v3
	v_ashrrev_i32_e32 v5, 8, v5
	v_mov_b32_e32 v10, s2
	v_readlane_b32 s2, v254, 8
	v_add_u32_e32 v5, v5, v4
	s_waitcnt vmcnt(0)
	ds_write_b128 v10, v[6:9]
	v_mov_b32_e32 v6, s2
	ds_write_b128 v6, v[2:5]
	v_mov_b32_e32 v6, v166
	v_mov_b32_e32 v7, v167
	v_mov_b32_e32 v8, v168
	v_add_u32_e32 v2, 0xff, v9
	v_ashrrev_i32_e32 v3, 31, v2
	v_add_u32_sdwa v2, v2, v3 dst_sel:DWORD dst_unused:UNUSED_PAD src0_sel:DWORD src1_sel:BYTE_3
	v_ashrrev_i32_e32 v2, 8, v2
	v_add_u32_e32 v2, v2, v5
	v_readlane_b32 s2, v254, 9
	s_waitcnt vmcnt(2)
	v_add_u32_e32 v3, 0xff, v6
	v_ashrrev_i32_e32 v4, 31, v3
	v_add_u32_sdwa v3, v3, v4 dst_sel:DWORD dst_unused:UNUSED_PAD src0_sel:DWORD src1_sel:BYTE_3
	s_waitcnt vmcnt(1)
	v_add_u32_e32 v4, 0xff, v7
	v_ashrrev_i32_e32 v5, 31, v4
	v_add_u32_sdwa v4, v4, v5 dst_sel:DWORD dst_unused:UNUSED_PAD src0_sel:DWORD src1_sel:BYTE_3
	s_waitcnt vmcnt(0)
	v_add_u32_e32 v5, 0xff, v8
	v_ashrrev_i32_e32 v9, 31, v5
	v_add_u32_sdwa v5, v5, v9 dst_sel:DWORD dst_unused:UNUSED_PAD src0_sel:DWORD src1_sel:BYTE_3
	v_mov_b32_e32 v9, v169
	v_ashrrev_i32_e32 v3, 8, v3
	v_add_u32_e32 v3, v3, v2
	v_ashrrev_i32_e32 v4, 8, v4
	v_add_u32_e32 v4, v4, v3
	v_ashrrev_i32_e32 v5, 8, v5
	v_mov_b32_e32 v10, s2
	v_readlane_b32 s2, v254, 10
	v_add_u32_e32 v5, v5, v4
	s_waitcnt vmcnt(0)
	ds_write_b128 v10, v[6:9]
	v_mov_b32_e32 v6, s2
	ds_write_b128 v6, v[2:5]
	v_mov_b32_e32 v6, v170
	v_mov_b32_e32 v7, v171
	v_mov_b32_e32 v8, v172
	v_add_u32_e32 v2, 0xff, v9
	v_ashrrev_i32_e32 v3, 31, v2
	v_add_u32_sdwa v2, v2, v3 dst_sel:DWORD dst_unused:UNUSED_PAD src0_sel:DWORD src1_sel:BYTE_3
	v_ashrrev_i32_e32 v2, 8, v2
	v_add_u32_e32 v2, v2, v5
	v_readlane_b32 s2, v254, 11
	s_waitcnt vmcnt(2)
	v_add_u32_e32 v3, 0xff, v6
	v_ashrrev_i32_e32 v4, 31, v3
	v_add_u32_sdwa v3, v3, v4 dst_sel:DWORD dst_unused:UNUSED_PAD src0_sel:DWORD src1_sel:BYTE_3
	s_waitcnt vmcnt(1)
	v_add_u32_e32 v4, 0xff, v7
	v_ashrrev_i32_e32 v5, 31, v4
	v_add_u32_sdwa v4, v4, v5 dst_sel:DWORD dst_unused:UNUSED_PAD src0_sel:DWORD src1_sel:BYTE_3
	s_waitcnt vmcnt(0)
	v_add_u32_e32 v5, 0xff, v8
	v_ashrrev_i32_e32 v9, 31, v5
	v_add_u32_sdwa v5, v5, v9 dst_sel:DWORD dst_unused:UNUSED_PAD src0_sel:DWORD src1_sel:BYTE_3
	v_mov_b32_e32 v9, v173
	v_ashrrev_i32_e32 v3, 8, v3
	v_add_u32_e32 v3, v3, v2
	v_ashrrev_i32_e32 v4, 8, v4
	v_add_u32_e32 v4, v4, v3
	v_ashrrev_i32_e32 v5, 8, v5
	v_mov_b32_e32 v10, s2
	v_readlane_b32 s2, v254, 12
	v_add_u32_e32 v5, v5, v4
	s_waitcnt vmcnt(0)
	ds_write_b128 v10, v[6:9]
	v_mov_b32_e32 v6, s2
	ds_write_b128 v6, v[2:5]
	v_mov_b32_e32 v6, v174
	v_mov_b32_e32 v7, v175
	v_mov_b32_e32 v8, v176
	v_add_u32_e32 v2, 0xff, v9
	v_ashrrev_i32_e32 v3, 31, v2
	v_add_u32_sdwa v2, v2, v3 dst_sel:DWORD dst_unused:UNUSED_PAD src0_sel:DWORD src1_sel:BYTE_3
	v_ashrrev_i32_e32 v2, 8, v2
	v_add_u32_e32 v2, v2, v5
	v_readlane_b32 s2, v254, 13
	s_waitcnt vmcnt(2)
	v_add_u32_e32 v3, 0xff, v6
	v_ashrrev_i32_e32 v4, 31, v3
	v_add_u32_sdwa v3, v3, v4 dst_sel:DWORD dst_unused:UNUSED_PAD src0_sel:DWORD src1_sel:BYTE_3
	s_waitcnt vmcnt(1)
	v_add_u32_e32 v4, 0xff, v7
	v_ashrrev_i32_e32 v5, 31, v4
	v_add_u32_sdwa v4, v4, v5 dst_sel:DWORD dst_unused:UNUSED_PAD src0_sel:DWORD src1_sel:BYTE_3
	s_waitcnt vmcnt(0)
	v_add_u32_e32 v5, 0xff, v8
	v_ashrrev_i32_e32 v9, 31, v5
	v_add_u32_sdwa v5, v5, v9 dst_sel:DWORD dst_unused:UNUSED_PAD src0_sel:DWORD src1_sel:BYTE_3
	v_mov_b32_e32 v9, v177
	v_ashrrev_i32_e32 v3, 8, v3
	v_add_u32_e32 v3, v3, v2
	v_ashrrev_i32_e32 v4, 8, v4
	v_add_u32_e32 v4, v4, v3
	v_ashrrev_i32_e32 v5, 8, v5
	v_mov_b32_e32 v10, s2
	v_readlane_b32 s2, v254, 14
	v_add_u32_e32 v5, v5, v4
	s_waitcnt vmcnt(0)
	ds_write_b128 v10, v[6:9]
	v_mov_b32_e32 v6, s2
	ds_write_b128 v6, v[2:5]
	v_mov_b32_e32 v6, v180
	v_mov_b32_e32 v7, v181
	v_mov_b32_e32 v8, v182
	v_add_u32_e32 v2, 0xff, v9
	v_ashrrev_i32_e32 v3, 31, v2
	v_add_u32_sdwa v2, v2, v3 dst_sel:DWORD dst_unused:UNUSED_PAD src0_sel:DWORD src1_sel:BYTE_3
	v_ashrrev_i32_e32 v2, 8, v2
	v_add_u32_e32 v2, v2, v5
	v_readlane_b32 s2, v254, 15
	s_waitcnt vmcnt(2)
	v_add_u32_e32 v3, 0xff, v6
	v_ashrrev_i32_e32 v4, 31, v3
	v_add_u32_sdwa v3, v3, v4 dst_sel:DWORD dst_unused:UNUSED_PAD src0_sel:DWORD src1_sel:BYTE_3
	s_waitcnt vmcnt(1)
	v_add_u32_e32 v4, 0xff, v7
	v_ashrrev_i32_e32 v5, 31, v4
	v_add_u32_sdwa v4, v4, v5 dst_sel:DWORD dst_unused:UNUSED_PAD src0_sel:DWORD src1_sel:BYTE_3
	s_waitcnt vmcnt(0)
; DEV void moe_tables(const Params& p, int layer, LAS int* bs, LAS int* cn) {
;     ...
;     if (threadIdx.x == 0) { int a = 0; for (int e = 0; e < 64; ++e) { const int c = (int)cnt[e * 32]; cn[e] = c; bs[e] = a; a += (c + MOE_RB - 1) / MOE_RB; } bs[64] = a; }
;     __syncthreads();
	v_add_u32_e32 v5, 0xff, v8
	v_ashrrev_i32_e32 v9, 31, v5
	v_add_u32_sdwa v5, v5, v9 dst_sel:DWORD dst_unused:UNUSED_PAD src0_sel:DWORD src1_sel:BYTE_3
	v_mov_b32_e32 v9, v183
	v_ashrrev_i32_e32 v3, 8, v3
	v_add_u32_e32 v3, v3, v2
	v_ashrrev_i32_e32 v4, 8, v4
	v_add_u32_e32 v4, v4, v3
	v_ashrrev_i32_e32 v5, 8, v5
	v_mov_b32_e32 v10, s2
	v_readlane_b32 s2, v254, 16
	v_add_u32_e32 v5, v5, v4
	s_waitcnt vmcnt(0)
	ds_write_b128 v10, v[6:9]
	v_mov_b32_e32 v6, s2
	ds_write_b128 v6, v[2:5]
	v_mov_b32_e32 v6, v184
	v_mov_b32_e32 v7, v185
	v_mov_b32_e32 v8, v186
	v_add_u32_e32 v2, 0xff, v9
	v_ashrrev_i32_e32 v3, 31, v2
	v_add_u32_sdwa v2, v2, v3 dst_sel:DWORD dst_unused:UNUSED_PAD src0_sel:DWORD src1_sel:BYTE_3
	v_ashrrev_i32_e32 v2, 8, v2
	v_add_u32_e32 v2, v2, v5
	v_readlane_b32 s2, v254, 17
	s_waitcnt vmcnt(2)
	v_add_u32_e32 v3, 0xff, v6
	v_ashrrev_i32_e32 v4, 31, v3
	v_add_u32_sdwa v3, v3, v4 dst_sel:DWORD dst_unused:UNUSED_PAD src0_sel:DWORD src1_sel:BYTE_3
	s_waitcnt vmcnt(1)
	v_add_u32_e32 v4, 0xff, v7
	v_ashrrev_i32_e32 v5, 31, v4
	v_add_u32_sdwa v4, v4, v5 dst_sel:DWORD dst_unused:UNUSED_PAD src0_sel:DWORD src1_sel:BYTE_3
	s_waitcnt vmcnt(0)
	v_add_u32_e32 v5, 0xff, v8
	v_ashrrev_i32_e32 v9, 31, v5
	v_add_u32_sdwa v5, v5, v9 dst_sel:DWORD dst_unused:UNUSED_PAD src0_sel:DWORD src1_sel:BYTE_3
	v_mov_b32_e32 v9, v188
	v_ashrrev_i32_e32 v3, 8, v3
	v_add_u32_e32 v3, v3, v2
	v_ashrrev_i32_e32 v4, 8, v4
	v_add_u32_e32 v4, v4, v3
	v_ashrrev_i32_e32 v5, 8, v5
	v_mov_b32_e32 v10, s2
	v_readlane_b32 s2, v254, 18
	v_add_u32_e32 v5, v5, v4
	s_waitcnt vmcnt(0)
	ds_write_b128 v10, v[6:9]
	v_mov_b32_e32 v6, s2
	ds_write_b128 v6, v[2:5]
	v_mov_b32_e32 v6, v189
	v_mov_b32_e32 v7, v198
	v_mov_b32_e32 v8, v199
	v_add_u32_e32 v2, 0xff, v9
	v_ashrrev_i32_e32 v3, 31, v2
	v_add_u32_sdwa v2, v2, v3 dst_sel:DWORD dst_unused:UNUSED_PAD src0_sel:DWORD src1_sel:BYTE_3
	v_ashrrev_i32_e32 v2, 8, v2
	v_add_u32_e32 v2, v2, v5
	v_readlane_b32 s2, v254, 19
	s_waitcnt vmcnt(2)
	v_add_u32_e32 v3, 0xff, v6
	v_ashrrev_i32_e32 v4, 31, v3
	v_add_u32_sdwa v3, v3, v4 dst_sel:DWORD dst_unused:UNUSED_PAD src0_sel:DWORD src1_sel:BYTE_3
	s_waitcnt vmcnt(1)
	v_add_u32_e32 v4, 0xff, v7
	v_ashrrev_i32_e32 v5, 31, v4
	v_add_u32_sdwa v4, v4, v5 dst_sel:DWORD dst_unused:UNUSED_PAD src0_sel:DWORD src1_sel:BYTE_3
	s_waitcnt vmcnt(0)
	v_add_u32_e32 v5, 0xff, v8
	v_ashrrev_i32_e32 v9, 31, v5
	v_add_u32_sdwa v5, v5, v9 dst_sel:DWORD dst_unused:UNUSED_PAD src0_sel:DWORD src1_sel:BYTE_3
	v_mov_b32_e32 v9, v200
	v_ashrrev_i32_e32 v3, 8, v3
	v_add_u32_e32 v3, v3, v2
	v_ashrrev_i32_e32 v4, 8, v4
	v_add_u32_e32 v4, v4, v3
	v_ashrrev_i32_e32 v5, 8, v5
	v_mov_b32_e32 v10, s2
	v_readlane_b32 s2, v254, 20
	v_add_u32_e32 v5, v5, v4
	s_waitcnt vmcnt(0)
	ds_write_b128 v10, v[6:9]
	v_mov_b32_e32 v6, s2
	ds_write_b128 v6, v[2:5]
	v_mov_b32_e32 v6, v201
	v_mov_b32_e32 v7, v202
	v_mov_b32_e32 v8, v203
	v_add_u32_e32 v2, 0xff, v9
	v_ashrrev_i32_e32 v3, 31, v2
	v_add_u32_sdwa v2, v2, v3 dst_sel:DWORD dst_unused:UNUSED_PAD src0_sel:DWORD src1_sel:BYTE_3
	v_ashrrev_i32_e32 v2, 8, v2
	v_add_u32_e32 v2, v2, v5
	v_readlane_b32 s2, v254, 21
	s_waitcnt vmcnt(2)
	v_add_u32_e32 v3, 0xff, v6
	v_ashrrev_i32_e32 v4, 31, v3
	v_add_u32_sdwa v3, v3, v4 dst_sel:DWORD dst_unused:UNUSED_PAD src0_sel:DWORD src1_sel:BYTE_3
	s_waitcnt vmcnt(1)
	v_add_u32_e32 v4, 0xff, v7
	v_ashrrev_i32_e32 v5, 31, v4
	v_add_u32_sdwa v4, v4, v5 dst_sel:DWORD dst_unused:UNUSED_PAD src0_sel:DWORD src1_sel:BYTE_3
	s_waitcnt vmcnt(0)
	v_add_u32_e32 v5, 0xff, v8
	v_ashrrev_i32_e32 v9, 31, v5
	v_add_u32_sdwa v5, v5, v9 dst_sel:DWORD dst_unused:UNUSED_PAD src0_sel:DWORD src1_sel:BYTE_3
	v_mov_b32_e32 v9, v204
	v_ashrrev_i32_e32 v3, 8, v3
	v_add_u32_e32 v3, v3, v2
	v_ashrrev_i32_e32 v4, 8, v4
	v_add_u32_e32 v4, v4, v3
	v_ashrrev_i32_e32 v5, 8, v5
	v_mov_b32_e32 v10, s2
	v_readlane_b32 s2, v254, 22
	v_add_u32_e32 v5, v5, v4
	s_waitcnt vmcnt(0)
	ds_write_b128 v10, v[6:9]
	v_mov_b32_e32 v6, s2
	ds_write_b128 v6, v[2:5]
	v_mov_b32_e32 v6, v205
	v_mov_b32_e32 v7, v206
	v_mov_b32_e32 v8, v207
	v_add_u32_e32 v2, 0xff, v9
	v_ashrrev_i32_e32 v3, 31, v2
	v_add_u32_sdwa v2, v2, v3 dst_sel:DWORD dst_unused:UNUSED_PAD src0_sel:DWORD src1_sel:BYTE_3
	v_ashrrev_i32_e32 v2, 8, v2
	v_add_u32_e32 v2, v2, v5
	v_readlane_b32 s2, v254, 23
	s_waitcnt vmcnt(2)
	v_add_u32_e32 v3, 0xff, v6
	v_ashrrev_i32_e32 v4, 31, v3
	v_add_u32_sdwa v3, v3, v4 dst_sel:DWORD dst_unused:UNUSED_PAD src0_sel:DWORD src1_sel:BYTE_3
	s_waitcnt vmcnt(1)
	v_add_u32_e32 v4, 0xff, v7
	v_ashrrev_i32_e32 v5, 31, v4
	v_add_u32_sdwa v4, v4, v5 dst_sel:DWORD dst_unused:UNUSED_PAD src0_sel:DWORD src1_sel:BYTE_3
	s_waitcnt vmcnt(0)
	v_add_u32_e32 v5, 0xff, v8
	v_ashrrev_i32_e32 v9, 31, v5
	v_add_u32_sdwa v5, v5, v9 dst_sel:DWORD dst_unused:UNUSED_PAD src0_sel:DWORD src1_sel:BYTE_3
	v_mov_b32_e32 v9, v210
	v_ashrrev_i32_e32 v3, 8, v3
	v_add_u32_e32 v3, v3, v2
	v_ashrrev_i32_e32 v4, 8, v4
	v_add_u32_e32 v4, v4, v3
	v_ashrrev_i32_e32 v5, 8, v5
	v_mov_b32_e32 v10, s2
	v_readlane_b32 s2, v254, 24
	v_add_u32_e32 v5, v5, v4
	s_waitcnt vmcnt(0)
	ds_write_b128 v10, v[6:9]
	v_mov_b32_e32 v6, s2
	ds_write_b128 v6, v[2:5]
	v_add_u32_e32 v2, 0xff, v9
	v_ashrrev_i32_e32 v3, 31, v2
	v_add_u32_sdwa v2, v2, v3 dst_sel:DWORD dst_unused:UNUSED_PAD src0_sel:DWORD src1_sel:BYTE_3
	v_ashrrev_i32_e32 v2, 8, v2
	v_readlane_b32 s2, v254, 25
	v_add_u32_e32 v2, v2, v5
	s_nop 0
	v_mov_b32_e32 v3, s2
	ds_write_b32 v3, v2
